# U phase: the 16-row LDS-DMA issue chain of a full chunk is straight-line (one m0 write per row, no per-row compare/branch); partial chunks keep the original chain
# speedup vs baseline: 1.0047x; 1.0015x over previous
; template <int VAR> __device__ __forceinline__ void u_process_grp(const UGrp& d, const v4u (&xb)[16], int j, size_t t0, int lane, LAS unsigned char* wl, const unsigned char* __restrict__ UT, const float* __restrict__ egate, unsigned* __restrict__ PW) {
;     ...
;     if (n == 0) return;
;     asm volatile("s_waitcnt lgkmcnt(0)" ::: "memory");
;     const size_t blk = t0 >> 6; const int tk0 = (int)(t0 & 63);
;     const unsigned wl_addr = (unsigned)(uintptr_t)wl;
;     ...
;     asm volatile("s_waitcnt lgkmcnt(0)" ::: "memory");
;     U_ISSUE(0);
.LBB0_689:
	s_or_b64 exec, exec, s[6:7]
	s_bcnt1_i32_b64 s6, vcc
	s_add_i32 s51, s51, s6
	s_cmp_eq_u32 s51, 0
	s_cbranch_scc1 .LBB0_751
	s_waitcnt lgkmcnt(0)
	s_waitcnt lgkmcnt(0)
	v_mov_b32_e32 v108, s25
	ds_read_b128 v[100:103], v108 offset:16400
	s_waitcnt lgkmcnt(1)
	ds_read_b128 v[96:99], v108 offset:16384
	ds_read_b128 v[104:107], v108 offset:16416
	ds_read_b128 v[108:111], v108 offset:16432
	s_cmp_eq_u32 s51, 1
	s_waitcnt lgkmcnt(3)
	v_readfirstlane_b32 s10, v100
	s_waitcnt lgkmcnt(2)
	v_lshlrev_b32_e32 v96, 10, v96
	v_and_b32_e32 v140, 0xfffc00, v96
	v_readfirstlane_b32 s58, v101
	v_lshl_add_u64 v[100:101], v[144:145], 0, v[140:141]
	s_mov_b32 s34, m0
	s_mov_b32 m0, s25
	s_nop 0
	global_load_lds_dwordx4 v[100:101], off
	s_mov_b32 m0, s34
	v_readfirstlane_b32 s57, v102
	v_readfirstlane_b32 s56, v103
	s_waitcnt lgkmcnt(1)
	v_readfirstlane_b32 s55, v104
	v_readfirstlane_b32 s54, v105
	v_readfirstlane_b32 s53, v106
	v_readfirstlane_b32 s52, v107
	s_waitcnt lgkmcnt(0)
	v_readfirstlane_b32 s49, v108
	v_readfirstlane_b32 s48, v109
	v_readfirstlane_b32 s7, v110
	v_readfirstlane_b32 s6, v111
	s_cmp_lt_u32 s51, 16
	s_cbranch_scc0 .Lufast_2
	s_cmp_eq_u32 s51, 1
	s_cbranch_scc0 .LBB0_831
	s_cmp_lt_u32 s51, 3
	s_cbranch_scc0 .LBB0_832

; #define LAS __attribute__((address_space(3)))
; template <int VAR> __device__ __forceinline__ void u_process_grp(const UGrp& d, const v4u (&xb)[16], int j, size_t t0, int lane, LAS unsigned char* wl, const unsigned char* __restrict__ UT, const float* __restrict__ egate, unsigned* __restrict__ PW) {
;     ...
;         for (int cc = 0; cc < 4; ++cc) {
;             const int c0 = s0 + 16 * cc;
;             if (c0 < n) {
;                 asm volatile("s_waitcnt vmcnt(0)" ::: "memory");
;                 f32x4 acc = (f32x4){0.f, 0.f, 0.f, 0.f};
;                 {   v4u ra[8];
; #pragma unroll
;                     for (int i = 0; i < 8; ++i) ra[i] = *(const LAS v4u*)(wl + r * 1024 + (((16 * g + i) ^ r) << 4));
; #pragma unroll
;                     for (int i = 0; i < 8; ++i) {
;                         acc = __builtin_amdgcn_mfma_f32_16x16x32_fp8_fp8((long)(((unsigned long long)ra[i].y << 32) | ra[i].x), (long)(((unsigned long long)xb[i].y << 32) | xb[i].x), acc, 0, 0, 0);
;                         acc = __builtin_amdgcn_mfma_f32_16x16x32_fp8_fp8((long)(((unsigned long long)ra[i].w << 32) | ra[i].z), (long)(((unsigned long long)xb[i].w << 32) | xb[i].z), acc, 0, 0, 0); } }
;                 {   v4u ra[8];
; #pragma unroll
;                     for (int i = 0; i < 8; ++i) ra[i] = *(const LAS v4u*)(wl + r * 1024 + (((16 * g + 8 + i) ^ r) << 4));
;                     asm volatile("s_waitcnt lgkmcnt(0)" ::: "memory");
;                     if (c0 + 16 < n) U_ISSUE(c0 + 16);
.LBB0_712:
	s_add_i32 s6, s52, s55
	s_cmp_ge_u32 s6, s51
	s_cbranch_scc1 .LBB0_711
	s_waitcnt vmcnt(0)
	v_add_u32_e32 v96, v143, v142
	s_waitcnt lgkmcnt(0)
	ds_read_b128 v[96:99], v96
	v_add_u32_e32 v100, v143, v180
	ds_read_b128 v[100:103], v100
	v_add_u32_e32 v108, v143, v186
	v_add_u32_e32 v109, v143, v187
	v_add_u32_e32 v110, v143, v188
	v_add_u32_e32 v111, v143, v189
	v_add_u32_e32 v132, v143, v192
	s_waitcnt lgkmcnt(1)
	v_mfma_f32_16x16x32_fp8_fp8 v[104:107], v[96:97], v[32:33], 0
	v_add_u32_e32 v140, v143, v193
	v_add_u32_e32 v236, v143, v194
	s_add_i32 s7, s6, 16
	v_mfma_f32_16x16x32_fp8_fp8 v[96:99], v[98:99], v[34:35], v[104:107]
	s_cmp_ge_u32 s7, s51
	ds_read_b128 v[128:131], v108
	s_waitcnt lgkmcnt(1)
	v_mfma_f32_16x16x32_fp8_fp8 v[96:99], v[100:101], v[36:37], v[96:99]
	v_add_u32_e32 v100, v143, v181
	v_add_u32_e32 v104, v143, v182
	ds_read_b128 v[104:107], v104
	v_mfma_f32_16x16x32_fp8_fp8 v[96:99], v[102:103], v[38:39], v[96:99]
	ds_read_b128 v[100:103], v100
	s_waitcnt lgkmcnt(0)
	v_mfma_f32_16x16x32_fp8_fp8 v[96:99], v[100:101], v[40:41], v[96:99]
	v_add_u32_e32 v100, v143, v183
	v_mfma_f32_16x16x32_fp8_fp8 v[96:99], v[102:103], v[42:43], v[96:99]
	ds_read_b128 v[100:103], v100
	v_mfma_f32_16x16x32_fp8_fp8 v[96:99], v[104:105], v[44:45], v[96:99]
	v_add_u32_e32 v104, v143, v184
	v_mfma_f32_16x16x32_fp8_fp8 v[96:99], v[106:107], v[46:47], v[96:99]
	ds_read_b128 v[104:107], v104
	s_waitcnt lgkmcnt(1)
	v_mfma_f32_16x16x32_fp8_fp8 v[96:99], v[100:101], v[48:49], v[96:99]
	v_add_u32_e32 v100, v143, v185
	v_mfma_f32_16x16x32_fp8_fp8 v[96:99], v[102:103], v[50:51], v[96:99]
	ds_read_b128 v[100:103], v100
	ds_read_b128 v[124:127], v109
	ds_read_b128 v[120:123], v110
	s_waitcnt lgkmcnt(3)
	v_mfma_f32_16x16x32_fp8_fp8 v[96:99], v[104:105], v[52:53], v[96:99]
	v_add_u32_e32 v104, v143, v190
	v_add_u32_e32 v105, v143, v191
	v_mfma_f32_16x16x32_fp8_fp8 v[96:99], v[106:107], v[54:55], v[96:99]
	ds_read_b128 v[116:119], v111
	ds_read_b128 v[112:115], v104
	ds_read_b128 v[108:111], v105
	ds_read_b128 v[104:107], v132
	s_waitcnt lgkmcnt(6)
	v_mfma_f32_16x16x32_fp8_fp8 v[96:99], v[100:101], v[56:57], v[96:99]
	v_mfma_f32_16x16x32_fp8_fp8 v[96:99], v[102:103], v[58:59], v[96:99]
	v_mfma_f32_16x16x32_fp8_fp8 v[132:135], v[128:129], v[60:61], v[96:99]
	ds_read_b128 v[100:103], v140
	s_nop 5
	ds_read_b128 v[96:99], v236
	s_waitcnt lgkmcnt(0)
	v_mfma_f32_16x16x32_fp8_fp8 v[128:131], v[130:131], v[62:63], v[132:135]
	s_cbranch_scc1 .LBB0_730
	v_mov_b32_e32 v140, s54
	ds_read_b128 v[236:239], v140 offset:16
	ds_read_b128 v[132:135], v140
	ds_read_b128 v[240:243], v140 offset:32
	ds_read_b128 v[244:247], v140 offset:48
	s_add_i32 s34, s6, 17
	s_waitcnt lgkmcnt(3)
	v_readfirstlane_b32 s10, v236
	s_waitcnt lgkmcnt(2)
	v_lshlrev_b32_e32 v132, 10, v132
	v_and_b32_e32 v140, 0xfffc00, v132
	v_readfirstlane_b32 s65, v237
	v_lshl_add_u64 v[236:237], v[144:145], 0, v[140:141]
	s_cmp_ge_u32 s34, s51
	s_mov_b32 s34, m0
	s_mov_b32 m0, s25
	s_nop 0
	global_load_lds_dwordx4 v[236:237], off
	s_mov_b32 m0, s34
	v_readfirstlane_b32 s64, v238
	v_readfirstlane_b32 s63, v239
	s_waitcnt lgkmcnt(1)
	v_readfirstlane_b32 s62, v240
	v_readfirstlane_b32 s59, v241
	v_readfirstlane_b32 s58, v242
	v_readfirstlane_b32 s57, v243
	s_waitcnt lgkmcnt(0)
	v_readfirstlane_b32 s56, v244
	v_readfirstlane_b32 s49, v245
	v_readfirstlane_b32 s48, v246
	v_readfirstlane_b32 s7, v247
	s_add_i32 s34, s6, 31
	s_cmp_ge_u32 s34, s51
	s_cbranch_scc0 .Lufast_0
	s_add_i32 s34, s6, 17
	s_cmp_ge_u32 s34, s51
	s_cbranch_scc0 .LBB0_735
	s_add_i32 s34, s6, 18
	s_cmp_ge_u32 s34, s51
	s_cbranch_scc0 .LBB0_736

.Lufast_0:
	s_mov_b32 s34, m0
	v_lshlrev_b32_e32 v132, 10, v133
	v_and_b32_e32 v140, 0xfffc00, v132
	s_add_i32 m0, s25, 0x400
	v_lshl_add_u64 v[132:133], v[146:147], 0, v[140:141]
	global_load_lds_dwordx4 v[132:133], off
	v_lshlrev_b32_e32 v132, 10, v134
	v_and_b32_e32 v140, 0xfffc00, v132
	s_add_i32 m0, s25, 0x800
	v_lshl_add_u64 v[132:133], v[148:149], 0, v[140:141]
	global_load_lds_dwordx4 v[132:133], off
	v_lshlrev_b32_e32 v132, 10, v135
	v_and_b32_e32 v140, 0xfffc00, v132
	s_add_i32 m0, s25, 0xc00
	v_lshl_add_u64 v[132:133], v[150:151], 0, v[140:141]
	global_load_lds_dwordx4 v[132:133], off
	s_lshl_b32 s10, s10, 10
	s_and_b32 s10, s10, 0xfffc00
	s_add_i32 m0, s25, 0x1000
	v_lshl_add_u64 v[132:133], v[152:153], 0, s[10:11]
	global_load_lds_dwordx4 v[132:133], off
	s_lshl_b32 s10, s65, 10
	s_and_b32 s10, s10, 0xfffc00
	s_add_i32 m0, s25, 0x1400
	v_lshl_add_u64 v[132:133], v[154:155], 0, s[10:11]
	global_load_lds_dwordx4 v[132:133], off
	s_lshl_b32 s10, s64, 10
	s_and_b32 s10, s10, 0xfffc00
	s_add_i32 m0, s25, 0x1800
	v_lshl_add_u64 v[132:133], v[156:157], 0, s[10:11]
	global_load_lds_dwordx4 v[132:133], off
	s_lshl_b32 s10, s63, 10
	s_and_b32 s10, s10, 0xfffc00
	s_add_i32 m0, s25, 0x1c00
	v_lshl_add_u64 v[132:133], v[158:159], 0, s[10:11]
	global_load_lds_dwordx4 v[132:133], off
	s_lshl_b32 s10, s62, 10
	s_and_b32 s10, s10, 0xfffc00
	s_add_i32 m0, s25, 0x2000
	v_lshl_add_u64 v[132:133], v[160:161], 0, s[10:11]
	global_load_lds_dwordx4 v[132:133], off
	s_lshl_b32 s10, s59, 10
	s_and_b32 s10, s10, 0xfffc00
	s_add_i32 m0, s25, 0x2400
	v_lshl_add_u64 v[132:133], v[162:163], 0, s[10:11]
	global_load_lds_dwordx4 v[132:133], off
	s_lshl_b32 s10, s58, 10
	s_and_b32 s10, s10, 0xfffc00
	s_add_i32 m0, s25, 0x2800
	v_lshl_add_u64 v[132:133], v[164:165], 0, s[10:11]
	global_load_lds_dwordx4 v[132:133], off
	s_lshl_b32 s10, s57, 10
	s_and_b32 s10, s10, 0xfffc00
	s_add_i32 m0, s25, 0x2c00
	v_lshl_add_u64 v[132:133], v[166:167], 0, s[10:11]
	global_load_lds_dwordx4 v[132:133], off
	s_lshl_b32 s10, s56, 10
	s_and_b32 s10, s10, 0xfffc00
	s_add_i32 m0, s25, 0x3000
	v_lshl_add_u64 v[132:133], v[168:169], 0, s[10:11]
	global_load_lds_dwordx4 v[132:133], off
	s_lshl_b32 s10, s49, 10
	s_and_b32 s10, s10, 0xfffc00
	s_add_i32 m0, s25, 0x3400
	v_lshl_add_u64 v[132:133], v[170:171], 0, s[10:11]
	global_load_lds_dwordx4 v[132:133], off
	s_lshl_b32 s10, s48, 10
	s_and_b32 s10, s10, 0xfffc00
	s_add_i32 m0, s25, 0x3800
	v_lshl_add_u64 v[132:133], v[172:173], 0, s[10:11]
	global_load_lds_dwordx4 v[132:133], off
	s_lshl_b32 s6, s7, 10
	s_and_b32 s10, s6, 0xfffc00
	s_add_i32 m0, s25, 0x3c00
	v_lshl_add_u64 v[132:133], v[174:175], 0, s[10:11]
	global_load_lds_dwordx4 v[132:133], off
	s_mov_b32 m0, s34
	s_branch .LBB0_730

; #define LAS __attribute__((address_space(3)))
; template <int VAR> __device__ __forceinline__ void u_process_grp(const UGrp& d, const v4u (&xb)[16], int j, size_t t0, int lane, LAS unsigned char* wl, const unsigned char* __restrict__ UT, const float* __restrict__ egate, unsigned* __restrict__ PW) {
;     ...
;         for (int cc = 0; cc < 4; ++cc) {
;             const int c0 = s0 + 16 * cc;
;             if (c0 < n) {
;                 asm volatile("s_waitcnt vmcnt(0)" ::: "memory");
;                 f32x4 acc = (f32x4){0.f, 0.f, 0.f, 0.f};
;                 {   v4u ra[8];
; #pragma unroll
;                     for (int i = 0; i < 8; ++i) ra[i] = *(const LAS v4u*)(wl + r * 1024 + (((16 * g + i) ^ r) << 4));
; #pragma unroll
;                     for (int i = 0; i < 8; ++i) {
;                         acc = __builtin_amdgcn_mfma_f32_16x16x32_fp8_fp8((long)(((unsigned long long)ra[i].y << 32) | ra[i].x), (long)(((unsigned long long)xb[i].y << 32) | xb[i].x), acc, 0, 0, 0);
;                         acc = __builtin_amdgcn_mfma_f32_16x16x32_fp8_fp8((long)(((unsigned long long)ra[i].w << 32) | ra[i].z), (long)(((unsigned long long)xb[i].w << 32) | xb[i].z), acc, 0, 0, 0); } }
;                 {   v4u ra[8];
; #pragma unroll
;                     for (int i = 0; i < 8; ++i) ra[i] = *(const LAS v4u*)(wl + r * 1024 + (((16 * g + 8 + i) ^ r) << 4));
;                     asm volatile("s_waitcnt lgkmcnt(0)" ::: "memory");
;                     if (c0 + 16 < n) U_ISSUE(c0 + 16);
.LBB0_792:
	s_add_i32 s6, s52, s55
	s_cmp_ge_u32 s6, s51
	s_cbranch_scc1 .LBB0_791
	s_waitcnt vmcnt(0)
	v_add_u32_e32 v96, v143, v142
	s_waitcnt lgkmcnt(0)
	ds_read_b128 v[96:99], v96
	v_add_u32_e32 v100, v143, v180
	ds_read_b128 v[100:103], v100
	v_add_u32_e32 v108, v143, v186
	v_add_u32_e32 v109, v143, v187
	v_add_u32_e32 v110, v143, v188
	v_add_u32_e32 v111, v143, v189
	v_add_u32_e32 v132, v143, v192
	s_waitcnt lgkmcnt(1)
	v_mfma_f32_16x16x32_fp8_fp8 v[104:107], v[96:97], v[32:33], 0
	v_add_u32_e32 v140, v143, v193
	v_add_u32_e32 v235, v143, v194
	s_add_i32 s7, s6, 16
	v_mfma_f32_16x16x32_fp8_fp8 v[96:99], v[98:99], v[34:35], v[104:107]
	s_cmp_ge_u32 s7, s51
	ds_read_b128 v[128:131], v108
	s_waitcnt lgkmcnt(1)
	v_mfma_f32_16x16x32_fp8_fp8 v[96:99], v[100:101], v[36:37], v[96:99]
	v_add_u32_e32 v100, v143, v181
	v_add_u32_e32 v104, v143, v182
	ds_read_b128 v[104:107], v104
	v_mfma_f32_16x16x32_fp8_fp8 v[96:99], v[102:103], v[38:39], v[96:99]
	ds_read_b128 v[100:103], v100
	s_waitcnt lgkmcnt(0)
	v_mfma_f32_16x16x32_fp8_fp8 v[96:99], v[100:101], v[40:41], v[96:99]
	v_add_u32_e32 v100, v143, v183
	v_mfma_f32_16x16x32_fp8_fp8 v[96:99], v[102:103], v[42:43], v[96:99]
	ds_read_b128 v[100:103], v100
	v_mfma_f32_16x16x32_fp8_fp8 v[96:99], v[104:105], v[44:45], v[96:99]
	v_add_u32_e32 v104, v143, v184
	v_mfma_f32_16x16x32_fp8_fp8 v[96:99], v[106:107], v[46:47], v[96:99]
	ds_read_b128 v[104:107], v104
	s_waitcnt lgkmcnt(1)
	v_mfma_f32_16x16x32_fp8_fp8 v[96:99], v[100:101], v[48:49], v[96:99]
	v_add_u32_e32 v100, v143, v185
	v_mfma_f32_16x16x32_fp8_fp8 v[96:99], v[102:103], v[50:51], v[96:99]
	ds_read_b128 v[100:103], v100
	ds_read_b128 v[124:127], v109
	ds_read_b128 v[120:123], v110
	s_waitcnt lgkmcnt(3)
	v_mfma_f32_16x16x32_fp8_fp8 v[96:99], v[104:105], v[52:53], v[96:99]
	v_add_u32_e32 v104, v143, v190
	v_add_u32_e32 v105, v143, v191
	v_mfma_f32_16x16x32_fp8_fp8 v[96:99], v[106:107], v[54:55], v[96:99]
	ds_read_b128 v[116:119], v111
	ds_read_b128 v[112:115], v104
	ds_read_b128 v[108:111], v105
	ds_read_b128 v[104:107], v132
	s_waitcnt lgkmcnt(6)
	v_mfma_f32_16x16x32_fp8_fp8 v[96:99], v[100:101], v[56:57], v[96:99]
	v_mfma_f32_16x16x32_fp8_fp8 v[96:99], v[102:103], v[58:59], v[96:99]
	v_mfma_f32_16x16x32_fp8_fp8 v[132:135], v[128:129], v[60:61], v[96:99]
	ds_read_b128 v[100:103], v140
	s_nop 5
	ds_read_b128 v[96:99], v235
	s_waitcnt lgkmcnt(0)
	v_mfma_f32_16x16x32_fp8_fp8 v[128:131], v[130:131], v[62:63], v[132:135]
	s_cbranch_scc1 .LBB0_810
	v_mov_b32_e32 v140, s54
	ds_read_b128 v[236:239], v140 offset:16
	ds_read_b128 v[132:135], v140
	ds_read_b128 v[240:243], v140 offset:32
	ds_read_b128 v[244:247], v140 offset:48
	s_add_i32 s34, s6, 17
	s_waitcnt lgkmcnt(3)
	v_readfirstlane_b32 s10, v236
	s_waitcnt lgkmcnt(2)
	v_lshlrev_b32_e32 v132, 10, v132
	v_and_b32_e32 v140, 0xfffc00, v132
	v_readfirstlane_b32 s65, v237
	v_lshl_add_u64 v[236:237], v[144:145], 0, v[140:141]
	s_cmp_ge_u32 s34, s51
	s_mov_b32 s34, m0
	s_mov_b32 m0, s25
	s_nop 0
	global_load_lds_dwordx4 v[236:237], off
	s_mov_b32 m0, s34
	v_readfirstlane_b32 s64, v238
	v_readfirstlane_b32 s63, v239
	s_waitcnt lgkmcnt(1)
	v_readfirstlane_b32 s62, v240
	v_readfirstlane_b32 s59, v241
	v_readfirstlane_b32 s58, v242
	v_readfirstlane_b32 s57, v243
	s_waitcnt lgkmcnt(0)
	v_readfirstlane_b32 s56, v244
	v_readfirstlane_b32 s49, v245
	v_readfirstlane_b32 s48, v246
	v_readfirstlane_b32 s7, v247
	s_add_i32 s34, s6, 31
	s_cmp_ge_u32 s34, s51
	s_cbranch_scc0 .Lufast_1
	s_add_i32 s34, s6, 17
	s_cmp_ge_u32 s34, s51
	s_cbranch_scc0 .LBB0_815
	s_add_i32 s34, s6, 18
	s_cmp_ge_u32 s34, s51
	s_cbranch_scc0 .LBB0_816

.Lufast_2:
	s_mov_b32 s34, m0
	v_lshlrev_b32_e32 v96, 10, v97
	v_and_b32_e32 v140, 0xfffc00, v96
	s_add_i32 m0, s25, 0x400
	v_lshl_add_u64 v[96:97], v[146:147], 0, v[140:141]
	global_load_lds_dwordx4 v[96:97], off
	v_lshlrev_b32_e32 v96, 10, v98
	v_and_b32_e32 v140, 0xfffc00, v96
	s_add_i32 m0, s25, 0x800
	v_lshl_add_u64 v[96:97], v[148:149], 0, v[140:141]
	global_load_lds_dwordx4 v[96:97], off
	v_lshlrev_b32_e32 v96, 10, v99
	v_and_b32_e32 v140, 0xfffc00, v96
	s_add_i32 m0, s25, 0xc00
	v_lshl_add_u64 v[96:97], v[150:151], 0, v[140:141]
	global_load_lds_dwordx4 v[96:97], off
	s_lshl_b32 s10, s10, 10
	s_and_b32 s10, s10, 0xfffc00
	s_add_i32 m0, s25, 0x1000
	v_lshl_add_u64 v[96:97], v[152:153], 0, s[10:11]
	global_load_lds_dwordx4 v[96:97], off
	s_lshl_b32 s10, s58, 10
	s_and_b32 s10, s10, 0xfffc00
	s_add_i32 m0, s25, 0x1400
	v_lshl_add_u64 v[96:97], v[154:155], 0, s[10:11]
	global_load_lds_dwordx4 v[96:97], off
	s_lshl_b32 s10, s57, 10
	s_and_b32 s10, s10, 0xfffc00
	s_add_i32 m0, s25, 0x1800
	v_lshl_add_u64 v[96:97], v[156:157], 0, s[10:11]
	global_load_lds_dwordx4 v[96:97], off
	s_lshl_b32 s10, s56, 10
	s_and_b32 s10, s10, 0xfffc00
	s_add_i32 m0, s25, 0x1c00
	v_lshl_add_u64 v[96:97], v[158:159], 0, s[10:11]
	global_load_lds_dwordx4 v[96:97], off
	s_lshl_b32 s10, s55, 10
	s_and_b32 s10, s10, 0xfffc00
	s_add_i32 m0, s25, 0x2000
	v_lshl_add_u64 v[96:97], v[160:161], 0, s[10:11]
	global_load_lds_dwordx4 v[96:97], off
	s_lshl_b32 s10, s54, 10
	s_and_b32 s10, s10, 0xfffc00
	s_add_i32 m0, s25, 0x2400
	v_lshl_add_u64 v[96:97], v[162:163], 0, s[10:11]
	global_load_lds_dwordx4 v[96:97], off
	s_lshl_b32 s10, s53, 10
	s_and_b32 s10, s10, 0xfffc00
	s_add_i32 m0, s25, 0x2800
	v_lshl_add_u64 v[96:97], v[164:165], 0, s[10:11]
	global_load_lds_dwordx4 v[96:97], off
	s_lshl_b32 s10, s52, 10
	s_and_b32 s10, s10, 0xfffc00
	s_add_i32 m0, s25, 0x2c00
	v_lshl_add_u64 v[96:97], v[166:167], 0, s[10:11]
	global_load_lds_dwordx4 v[96:97], off
	s_lshl_b32 s10, s49, 10
	s_and_b32 s10, s10, 0xfffc00
	s_add_i32 m0, s25, 0x3000
	v_lshl_add_u64 v[96:97], v[168:169], 0, s[10:11]
	global_load_lds_dwordx4 v[96:97], off
	s_lshl_b32 s10, s48, 10
	s_and_b32 s10, s10, 0xfffc00
	s_add_i32 m0, s25, 0x3400
	v_lshl_add_u64 v[96:97], v[170:171], 0, s[10:11]
	global_load_lds_dwordx4 v[96:97], off
	s_lshl_b32 s7, s7, 10
	s_and_b32 s10, s7, 0xfffc00
	s_add_i32 m0, s25, 0x3800
	v_lshl_add_u64 v[96:97], v[172:173], 0, s[10:11]
	global_load_lds_dwordx4 v[96:97], off
	s_lshl_b32 s6, s6, 10
	s_and_b32 s10, s6, 0xfffc00
	s_add_i32 m0, s25, 0x3c00
	v_lshl_add_u64 v[96:97], v[174:175], 0, s[10:11]
	global_load_lds_dwordx4 v[96:97], off
	s_mov_b32 m0, s34
	s_branch .LBB0_706
